# MoE down-projection epilogue: the first row's routing-weight load is issued with the other fifteen row loads instead of inside the row's branch behind its own wait
# speedup vs baseline: 1.0079x; 1.0079x over previous
;     __device__ __forceinline__ void operator()(const f32x4 (&acc)[2][2][4][2], const Unit& u, int wr, int wc, int fr, int fq) const {
;         int av[2][4]; float wv[2][4];
; #pragma unroll
;         for (int ai = 0; ai < 2; ++ai)
; #pragma unroll
;             for (int m = 0; m < 4; ++m) { const int row = u.pm * 256 + 128 * ai + 64 * wr + 16 * m + fr; av[ai][m] = rowasg[row]; wv[ai][m] = roww[row] * OUTS_SCALE; }
; #pragma unroll
;         for (int ai = 0; ai < 2; ++ai)
; #pragma unroll
;             for (int m = 0; m < 4; ++m) {
;                 const int a = av[ai][m]; const float w = wv[ai][m];
;                 if (a >= 0) { unsigned char* rowp = O + (size_t)(a - asg0) * 1024 + u.pn * 256 + 32 * wc + 8 * fq;
; #pragma unroll
;                     for (int bj = 0; bj < 2; ++bj) { f32x4 x0 = acc[ai][bj][m][0] * w, x1 = acc[ai][bj][m][1] * w;
; #pragma unroll
;                         for (int e = 0; e < 4; ++e) { x0[e] = fminf(fmaxf(x0[e], -440.f), 440.f); x1[e] = fminf(fmaxf(x1[e], -440.f), 440.f); }
;                         int w0 = __builtin_amdgcn_cvt_pk_fp8_f32(x0[0], x0[1], 0, false); w0 = __builtin_amdgcn_cvt_pk_fp8_f32(x0[2], x0[3], w0, true);
;                         int w1 = __builtin_amdgcn_cvt_pk_fp8_f32(x1[0], x1[1], 0, false); w1 = __builtin_amdgcn_cvt_pk_fp8_f32(x1[2], x1[3], w1, true);
;                         u32x2 o; o.x = (unsigned)w0; o.y = (unsigned)w1; *(u32x2*)(rowp + bj * 128) = o; } }
.LBB0_2137:
	v_lshl_add_u32 v146, s59, 8, v155
	v_ashrrev_i32_e32 v147, 31, v146
	v_lshlrev_b64 v[146:147], 2, v[146:147]
	v_lshl_add_u64 v[172:173], s[24:25], 0, v[146:147]
	v_lshl_add_u64 v[146:147], s[26:27], 0, v[146:147]
	global_load_dword v160, v[172:173], off offset:64
	global_load_dword v158, v[172:173], off offset:128
	global_load_dword v156, v[172:173], off offset:192
	global_load_dword v153, v[172:173], off offset:512
	global_load_dword v149, v[172:173], off offset:576
	global_load_dword v145, v[172:173], off offset:640
	global_load_dword v134, v[172:173], off offset:704
	s_nop 0
	global_load_dword v172, v[172:173], off
	s_nop 0
	global_load_dword v161, v[146:147], off offset:64
	global_load_dword v159, v[146:147], off offset:128
	global_load_dword v157, v[146:147], off offset:192
	global_load_dword v154, v[146:147], off offset:512
	global_load_dword v152, v[146:147], off offset:576
	global_load_dword v148, v[146:147], off offset:640
	global_load_dword v143, v[146:147], off offset:704
	global_load_dword v254, v[146:147], off
	s_lshl_b32 s40, s64, 8
	s_ashr_i32 s41, s40, 31
	s_waitcnt vmcnt(0)
	v_cmp_lt_i32_e32 vcc, -1, v172
	s_and_saveexec_b64 s[6:7], vcc
	s_cbranch_execz .LBB0_2146
	v_mov_b32_e32 v146, v254
	s_waitcnt vmcnt(0)
	v_mul_f32_e32 v174, 0x42800000, v146
	v_pk_mul_f32 v[126:127], v[126:127], v[174:175] op_sel_hi:[1,0]
	v_pk_mul_f32 v[122:123], v[122:123], v[174:175] op_sel_hi:[1,0]
	v_subrev_u32_e32 v146, s68, v172
	v_med3_f32 v126, v126, s8, v169
	v_med3_f32 v172, v122, s8, v169
	v_med3_f32 v127, v127, s8, v169
	v_mov_b32_e32 v122, v135
	v_cvt_pk_fp8_f32 v122, v126, v127
	v_pk_mul_f32 v[128:129], v[128:129], v[174:175] op_sel_hi:[1,0]
	v_med3_f32 v173, v123, s8, v169
	v_med3_f32 v123, v128, s8, v169
	v_med3_f32 v128, v129, s8, v169
	v_cvt_pk_fp8_f32 v122, v123, v128 op_sel:[0,0,1]
	v_mov_b32_e32 v123, v135
	v_cvt_pk_fp8_f32 v123, v172, v173
	v_ashrrev_i32_e32 v147, 31, v146
	v_pk_mul_f32 v[124:125], v[124:125], v[174:175] op_sel_hi:[1,0]
	v_lshlrev_b64 v[146:147], 10, v[146:147]
	v_med3_f32 v124, v124, s8, v169
	v_med3_f32 v125, v125, s8, v169
	v_lshl_add_u64 v[146:147], s[66:67], 0, v[146:147]
	v_cvt_pk_fp8_f32 v123, v124, v125 op_sel:[0,0,1]
	v_lshl_add_u64 v[146:147], v[146:147], 0, s[40:41]
	v_lshl_add_u64 v[146:147], v[146:147], 0, s[16:17]
	v_lshl_add_u64 v[146:147], v[146:147], 0, v[140:141]
	v_pk_mul_f32 v[118:119], v[118:119], v[174:175] op_sel_hi:[1,0]
	v_pk_mul_f32 v[114:115], v[114:115], v[174:175] op_sel_hi:[1,0]
	global_store_dwordx2 v[146:147], v[122:123], off
	v_med3_f32 v118, v118, s8, v169
	v_med3_f32 v122, v114, s8, v169
	v_med3_f32 v119, v119, s8, v169
	v_mov_b32_e32 v114, v135
	v_cvt_pk_fp8_f32 v114, v118, v119
	v_pk_mul_f32 v[120:121], v[120:121], v[174:175] op_sel_hi:[1,0]
	v_med3_f32 v123, v115, s8, v169
	v_med3_f32 v115, v120, s8, v169
	v_med3_f32 v120, v121, s8, v169
	v_cvt_pk_fp8_f32 v114, v115, v120 op_sel:[0,0,1]
	v_mov_b32_e32 v115, v135
	v_cvt_pk_fp8_f32 v115, v122, v123
	v_pk_mul_f32 v[116:117], v[116:117], v[174:175] op_sel_hi:[1,0]
	s_nop 0
	v_med3_f32 v116, v116, s8, v169
	v_med3_f32 v117, v117, s8, v169
	v_cvt_pk_fp8_f32 v115, v116, v117 op_sel:[0,0,1]
	global_store_dwordx2 v[146:147], v[114:115], off offset:128
	s_or_b64 exec, exec, s[6:7]
	v_cmp_lt_i32_e32 vcc, -1, v160
	s_and_saveexec_b64 s[6:7], vcc
	s_cbranch_execnz .LBB0_2147
